# GEMM phase prologues (8 sites): the second K-tile's 6 LDS-DMA pieces are issued before the first wait/barrier (vmcnt(2)+barrier -> vmcnt(8)+barrier after them), so both prologue tiles fly together
# baseline (speedup 1.0000x reference)
.LBB0_254:
	s_lshl_b32 s6, s6, 5
	s_and_b32 s18, s6, 0x60
	s_lshl_b32 s16, s1, 13
	s_lshl_b32 s19, s18, 7
	s_add_u32 s6, s10, 0x80
	s_addc_u32 s7, s11, 0
	v_mov_b32_e32 v1, v220
	v_mov_b32_e32 v2, v221
	s_add_i32 m0, s91, 0x18000
	s_mov_b32 s35, 0
	global_load_lds_dwordx4 v1, s[6:7]
	s_add_i32 m0, s91, 0x1a000
	v_mov_b32_e32 v1, v223
	global_load_lds_dwordx4 v2, s[6:7]
	s_add_u32 s6, s8, 0x80
	s_addc_u32 s7, s9, 0
	s_add_i32 s82, s91, 0x8000
	v_mov_b32_e32 v2, v222
	s_mov_b32 m0, s82
	s_add_i32 s34, s91, 0xa000
	s_nop 0
	global_load_lds_dwordx4 v2, s[6:7]
	s_mov_b32 m0, s34
	v_mov_b32_e32 v2, v220
	global_load_lds_dwordx4 v1, s[6:7]
	s_add_u32 s6, s12, 0x80
	s_addc_u32 s7, s13, 0
	v_mov_b32_e32 v1, v221
	s_add_i32 m0, s91, 0x1c000
	s_nop 0
	global_load_lds_dwordx4 v2, s[6:7]
	s_add_i32 m0, s91, 0x1e000
	v_lshrrev_b32_e32 v2, 1, v0
	global_load_lds_dwordx4 v1, s[6:7]
	v_and_b32_e32 v2, 24, v2
	v_and_b32_e32 v1, 15, v0
	v_lshlrev_b32_e32 v3, 1, v2
	v_lshlrev_b32_e32 v0, 2, v0
	s_cmp_gt_i32 s33, 0
	v_lshl_or_b32 v224, s1, 6, v1
	v_lshl_or_b32 v1, v1, 6, v3
	v_and_b32_e32 v0, 32, v0
	s_waitcnt vmcnt(8)
	s_barrier
	s_waitcnt vmcnt(6)
	s_cselect_b64 s[48:49], -1, 0
	s_add_i32 s88, s33, -2
	v_bitop3_b32 v3, v1, s16, v0 bitop3:0xde
	s_cmpk_lt_u32 s0, 0x100
	v_bitop3_b32 v225, v1, s19, v0 bitop3:0xde
	s_cselect_b64 s[50:51], -1, 0
	v_or_b32_e32 v226, s18, v2
	v_add_u32_e32 v227, 0, v3
	s_barrier
	s_branch .LBB0_257

.LBB0_1212:
	s_add_u32 s12, s44, 0x80
	s_addc_u32 s13, s45, 0
	s_add_u32 s14, s36, 0x280
	s_addc_u32 s15, s37, 0
	s_add_u32 s16, s44, 0x40080
	s_addc_u32 s17, s45, 0
	v_mov_b32_e32 v1, v139
	v_mov_b32_e32 v2, v138
	s_add_i32 m0, s49, 0x18000
	s_add_i32 s56, s49, 0x8000
	global_load_lds_dwordx4 v2, s[12:13] nt
	s_add_i32 m0, s49, 0x1a000
	v_mov_b32_e32 v2, v130
	global_load_lds_dwordx4 v1, s[12:13] nt
	v_mov_b32_e32 v1, v128
	s_mov_b32 m0, s56
	s_add_i32 s57, s49, 0xa000
	s_lshl_b32 s7, s7, 5
	global_load_lds_dwordx4 v1, s[14:15] nt
	s_mov_b32 m0, s57
	v_mov_b32_e32 v1, v139
	global_load_lds_dwordx4 v2, s[14:15] nt
	v_mov_b32_e32 v2, v138
	s_add_i32 m0, s49, 0x1c000
	s_and_b32 s7, s7, 0x60
	global_load_lds_dwordx4 v2, s[16:17] nt
	s_add_i32 m0, s49, 0x1e000
	v_lshrrev_b32_e32 v2, 1, v0
	global_load_lds_dwordx4 v1, s[16:17] nt
	v_and_b32_e32 v2, 24, v2
	v_and_b32_e32 v1, 15, v0
	v_lshlrev_b32_e32 v3, 1, v2
	v_lshlrev_b32_e32 v0, 2, v0
	v_lshl_or_b32 v129, s10, 6, v1
	v_lshl_or_b32 v1, v1, 6, v3
	s_lshl_b32 s10, s10, 13
	v_and_b32_e32 v0, 32, v0
	v_bitop3_b32 v3, v1, s10, v0 bitop3:0xde
	s_lshl_b32 s10, s7, 7
	s_cmp_gt_i32 s3, 0
	v_bitop3_b32 v131, v1, s10, v0 bitop3:0xde
	s_cselect_b64 s[10:11], -1, 0
	s_add_i32 s58, s3, -2
	s_waitcnt vmcnt(8)
	s_barrier
	s_waitcnt vmcnt(6)
	s_cmpk_lt_u32 s6, 0x100
	s_cselect_b64 s[12:13], -1, 0
	s_add_i32 s59, 0, 0x10000
	s_add_i32 s60, 0, 0x14000
	v_or_b32_e32 v140, s7, v2
	v_add_u32_e32 v141, s59, v131
	s_mov_b32 s61, 0xc000
	v_add_u32_e32 v142, s60, v131
	v_add_u32_e32 v143, 0, v3
	s_mov_b32 s62, 0x30000
	s_mov_b32 s63, 0x36000
	s_mov_b32 s64, 0x3c000
	s_mov_b32 s65, 0x42000
	v_mov_b64_e32 v[132:133], 0x1ff
	v_mov_b32_e32 v144, 0xbbb906ce
	v_mov_b32_e32 v145, 0xbc3963d9
	s_barrier
	s_branch .LBB0_1215

.LBB0_1242:
	s_lshl_b32 s10, s10, 5
	s_and_b32 s17, s10, 0x60
	s_lshl_b32 s16, s7, 13
	s_lshl_b32 s18, s17, 7
	s_add_u32 s58, s26, 0x75000000
	s_addc_u32 s59, s27, 0
	s_lshl_b32 s10, s11, 1
	s_or_b32 s10, s10, s13
	s_mul_i32 s10, s10, 9
	s_add_i32 s10, s10, s12
	s_ashr_i32 s11, s10, 31
	s_lshl_b64 s[10:11], s[10:11], 17
	s_add_u32 s22, s58, s10
	s_addc_u32 s23, s59, s11
	s_add_u32 s10, s44, 0x80
	s_addc_u32 s11, s45, 0
	s_add_u32 s12, s38, 0x80
	s_addc_u32 s13, s39, 0
	s_add_u32 s14, s44, 0x900080
	s_addc_u32 s15, s45, 0
	v_mov_b32_e32 v1, v134
	v_mov_b32_e32 v2, v135
	s_add_i32 m0, s48, 0x18000
	s_add_i32 s60, s48, 0x8000
	global_load_lds_dwordx4 v1, s[10:11]
	s_add_i32 m0, s48, 0x1a000
	v_mov_b32_e32 v1, v130
	global_load_lds_dwordx4 v2, s[10:11]
	v_mov_b32_e32 v2, v128
	s_mov_b32 m0, s60
	s_add_i32 s61, s48, 0xa000
	v_mov_b64_e32 v[132:133], 0x3ff
	global_load_lds_dwordx4 v2, s[12:13] nt
	s_mov_b32 m0, s61
	v_mov_b32_e32 v2, v134
	global_load_lds_dwordx4 v1, s[12:13] nt
	v_mov_b32_e32 v1, v135
	s_add_i32 m0, s48, 0x1c000
	s_nop 0
	global_load_lds_dwordx4 v2, s[14:15]
	s_add_i32 m0, s48, 0x1e000
	v_lshrrev_b32_e32 v2, 1, v0
	global_load_lds_dwordx4 v1, s[14:15]
	v_and_b32_e32 v2, 24, v2
	s_cmp_gt_i32 s2, 0
	v_and_b32_e32 v1, 15, v0
	v_lshlrev_b32_e32 v3, 1, v2
	v_lshlrev_b32_e32 v0, 2, v0
	s_cselect_b64 s[10:11], -1, 0
	s_add_i32 s62, s2, -2
	v_lshl_or_b32 v129, s7, 6, v1
	v_lshl_or_b32 v1, v1, 6, v3
	v_and_b32_e32 v0, 32, v0
	s_waitcnt vmcnt(8)
	s_barrier
	s_waitcnt vmcnt(6)
	s_cmpk_lt_u32 s6, 0x100
	v_bitop3_b32 v3, v1, s16, v0 bitop3:0xde
	v_bitop3_b32 v131, v1, s18, v0 bitop3:0xde
	s_cselect_b64 s[12:13], -1, 0
	s_add_i32 s63, 0, 0x10000
	s_add_i32 s64, 0, 0x14000
	v_or_b32_e32 v136, s17, v2
	v_add_u32_e32 v137, s63, v131
	v_add_u32_e32 v138, s64, v131
	v_add_u32_e32 v139, 0, v3
	s_barrier
	s_branch .LBB0_1245

.LBB0_1266:
	s_add_u32 s63, s26, 0x34000000
	s_addc_u32 s64, s27, 0
	s_lshl_b64 s[28:29], s[48:49], 9
	s_lshl_b64 s[30:31], s[6:7], 21
	s_add_u32 s7, s63, s30
	s_addc_u32 s19, s64, s31
	s_add_u32 s50, s7, s28
	s_addc_u32 s51, s19, s29
	s_lshl_b32 s77, s6, 8
	s_lshl_b32 s6, s17, 5
	s_and_b32 s20, s6, 0x60
	s_lshl_b32 s19, s16, 13
	s_lshl_b32 s17, s20, 7
	s_add_u32 s49, s26, 0x950000
	s_addc_u32 s65, s27, 0
	s_add_u32 s6, s56, 0x80
	s_addc_u32 s7, s57, 0
	v_mov_b32_e32 v1, v182
	v_mov_b32_e32 v2, v183
	s_add_i32 m0, s33, 0x18000
	s_mov_b32 s68, 0
	global_load_lds_dwordx4 v1, s[6:7]
	s_add_i32 m0, s33, 0x1a000
	v_mov_b32_e32 v1, v185
	global_load_lds_dwordx4 v2, s[6:7]
	s_add_u32 s6, s52, 0x80
	s_addc_u32 s7, s53, 0
	s_add_i32 s66, s33, 0x8000
	v_mov_b32_e32 v2, v184
	s_mov_b32 m0, s66
	s_add_i32 s67, s33, 0xa000
	s_mov_b32 s22, 0x3fb8aa3b
	global_load_lds_dwordx4 v2, s[6:7]
	s_mov_b32 m0, s67
	v_mov_b32_e32 v2, v183
	global_load_lds_dwordx4 v1, s[6:7]
	s_add_u32 s6, s56, 0x8080
	s_addc_u32 s7, s57, 0
	v_mov_b32_e32 v1, v182
	s_add_i32 m0, s33, 0x1c000
	s_mov_b32 s72, 0x40000
	global_load_lds_dwordx4 v1, s[6:7]
	s_add_i32 m0, s33, 0x1e000
	v_and_b32_e32 v1, 15, v0
	global_load_lds_dwordx4 v2, s[6:7]
	v_lshrrev_b32_e32 v2, 1, v0
	v_and_b32_e32 v2, 24, v2
	v_lshlrev_b32_e32 v3, 1, v2
	v_lshlrev_b32_e32 v0, 2, v0
	v_lshl_or_b32 v186, s16, 6, v1
	v_lshl_or_b32 v1, v1, 6, v3
	v_and_b32_e32 v0, 32, v0
	s_cmp_gt_i32 s2, 0
	v_bitop3_b32 v187, v1, s17, v0 bitop3:0xde
	s_cselect_b64 s[16:17], -1, 0
	s_add_i32 s69, s2, -2
	s_waitcnt vmcnt(8)
	s_barrier
	s_waitcnt vmcnt(6)
	s_cmpk_lt_u32 s18, 0x100
	v_bitop3_b32 v3, v1, s19, v0 bitop3:0xde
	s_cselect_b64 s[18:19], -1, 0
	s_add_i32 s70, 0, 0x10000
	s_add_i32 s71, 0, 0x14000
	v_or_b32_e32 v188, s20, v2
	v_add_u32_e32 v189, s70, v187
	v_add_u32_e32 v190, s71, v187
	v_add_u32_e32 v191, 0, v3
	s_mov_b32 s20, 0xbfb8aa3b
	s_mov_b32 s73, 0x60000
	s_mov_b32 s74, 0x100000
	s_mov_b32 s75, 0x120000
	s_mov_b32 s76, 0x140000
	v_mov_b64_e32 v[156:157], 0x8ff
	s_barrier
	s_branch .LBB0_1269

.LBB0_1423:
	s_and_b32 s19, s7, 3
	s_load_dword s10, s[90:91], 0x100
	s_lshl_b32 s7, s6, 13
	s_lshl_b32 s9, s19, 12
	s_add_u32 s57, s26, 0x4e000000
	s_addc_u32 s58, s27, 0
	s_add_u32 s20, s26, 0x63800000
	s_addc_u32 s21, s27, 0
	s_waitcnt lgkmcnt(0)
	s_ashr_i32 s59, s10, 31
	s_add_u32 s10, s50, 0x80
	s_addc_u32 s11, s51, 0
	v_mov_b32_e32 v1, v214
	v_mov_b32_e32 v2, v215
	s_add_i32 m0, s33, 0x18000
	v_mov_b32_e32 v208, 0
	global_load_lds_dwordx4 v1, s[10:11] nt
	s_add_i32 m0, s33, 0x1a000
	v_mov_b32_e32 v1, v206
	global_load_lds_dwordx4 v2, s[10:11] nt
	s_add_u32 s10, s12, 0x80
	s_addc_u32 s11, s13, 0
	s_add_i32 s60, s33, 0x8000
	v_mov_b32_e32 v2, v204
	s_mov_b32 m0, s60
	s_add_i32 s61, s33, 0xa000
	s_mov_b32 s30, 0x3b800000
	global_load_lds_dwordx4 v2, s[10:11] nt
	s_mov_b32 m0, s61
	v_mov_b32_e32 v2, v215
	global_load_lds_dwordx4 v1, s[10:11] nt
	s_add_u32 s10, s48, 0x80
	s_addc_u32 s11, s49, 0
	v_mov_b32_e32 v1, v214
	s_add_i32 m0, s33, 0x1c000
	s_mov_b32 s73, 0xf800000
	global_load_lds_dwordx4 v1, s[10:11] nt
	s_add_i32 m0, s33, 0x1e000
	s_cmp_gt_i32 s3, 0
	global_load_lds_dwordx4 v2, s[10:11] nt
	v_bfe_u32 v2, v0, 4, 2
	s_cselect_b64 s[22:23], -1, 0
	s_add_i32 s62, s3, -2
	v_and_b32_e32 v1, 15, v0
	v_lshlrev_b32_e32 v4, 4, v2
	v_lshlrev_b32_e32 v0, 2, v0
	s_cmpk_lt_u32 s8, 0x100
	v_lshl_or_b32 v205, s6, 6, v1
	v_lshl_or_b32 v1, v1, 6, v4
	v_and_b32_e32 v0, 32, v0
	s_waitcnt vmcnt(8)
	s_barrier
	s_waitcnt vmcnt(6)
	s_cselect_b64 s[28:29], -1, 0
	s_lshl_b32 s10, s19, 3
	v_lshlrev_b32_e32 v3, 3, v2
	v_bitop3_b32 v4, v1, s7, v0 bitop3:0xde
	v_bitop3_b32 v207, v1, s9, v0 bitop3:0xde
	s_add_i32 s70, s10, 0
	s_add_i32 s71, 0, 0x10000
	s_add_i32 s72, 0, 0x14000
	v_mbcnt_lo_u32_b32 v0, -1, 0
	v_lshl_or_b32 v216, s19, 5, v3
	v_cmp_eq_u32_e64 s[6:7], 0, v2
	v_cmp_ne_u32_e64 s[8:9], 0, v2
	s_add_i32 s63, s70, 0x22000
	s_add_i32 s64, s70, 0x22200
	s_add_i32 s65, s70, 0x22400
	s_add_i32 s66, s70, 0x22600
	s_add_i32 s67, s70, 0x23000
	s_add_i32 s68, s70, 0x23200
	s_add_i32 s69, s70, 0x23400
	s_add_i32 s70, s70, 0x23600
	v_add_u32_e32 v217, s71, v207
	v_add_u32_e32 v218, s72, v207
	v_add_u32_e32 v219, 0, v4
	v_mbcnt_hi_u32_b32 v220, -1, v0
	v_mov_b32_e32 v221, 0x260
	v_mov_b64_e32 v[210:211], 0x1ff
	s_mov_b32 s75, 0
	s_barrier
	s_branch .LBB0_1426

.LBB0_1652:
	s_load_dword s8, s[90:91], 0x100
	s_add_u32 s14, s26, 0x3400000
	s_addc_u32 s15, s27, 0
	s_and_b32 s59, s7, 3
	s_ashr_i32 s58, s94, 31
	s_waitcnt lgkmcnt(0)
	s_ashr_i32 s57, s8, 31
	s_lshl_b32 s7, s6, 13
	s_lshl_b32 s17, s59, 12
	s_add_u32 s8, s48, 0x80
	s_addc_u32 s9, s49, 0
	v_mov_b32_e32 v0, v213
	v_mov_b32_e32 v1, v212
	s_add_i32 m0, s53, 0x18000
	s_mov_b64 s[22:23], 0x804000
	global_load_lds_dwordx4 v1, s[8:9]
	s_add_i32 m0, s53, 0x1a000
	v_mov_b32_e32 v1, v213
	global_load_lds_dwordx4 v0, s[8:9]
	s_add_u32 s8, s44, 0x80
	s_addc_u32 s9, s45, 0
	s_add_i32 s60, s53, 0x8000
	v_mov_b32_e32 v0, v212
	s_mov_b32 m0, s60
	s_add_i32 s61, s53, 0xa000
	s_mov_b32 s65, 0x804000
	global_load_lds_dwordx4 v0, s[8:9]
	s_mov_b32 m0, s61
	v_mov_b32_e32 v0, v213
	global_load_lds_dwordx4 v1, s[8:9]
	s_add_u32 s8, s46, 0x80
	s_addc_u32 s9, s47, 0
	v_mov_b32_e32 v1, v212
	s_add_i32 m0, s53, 0x1c000
	v_mov_b64_e32 v[192:193], 0x3ff
	global_load_lds_dwordx4 v1, s[8:9]
	s_add_i32 m0, s53, 0x1e000
	v_bfe_u32 v1, v2, 4, 2
	global_load_lds_dwordx4 v0, s[8:9]
	v_and_b32_e32 v0, 15, v2
	v_lshlrev_b32_e32 v3, 4, v1
	v_lshlrev_b32_e32 v2, 2, v2
	s_cmp_gt_i32 s33, 0
	v_lshl_or_b32 v214, s6, 6, v0
	v_lshl_or_b32 v0, v0, 6, v3
	v_and_b32_e32 v2, 32, v2
	s_cselect_b64 s[18:19], -1, 0
	s_add_i32 s62, s33, -2
	v_bitop3_b32 v3, v0, s7, v2 bitop3:0xde
	v_bitop3_b32 v215, v0, s17, v2 bitop3:0xde
	s_waitcnt vmcnt(8)
	s_barrier
	s_waitcnt vmcnt(6)
	s_cmpk_lt_u32 s20, 0x100
	v_lshlrev_b32_e32 v0, 2, v1
	s_cselect_b64 s[20:21], -1, 0
	v_lshl_or_b32 v216, s59, 5, v0
	s_add_i32 s63, 0, 0x10000
	s_add_i32 s64, 0, 0x14000
	v_mbcnt_lo_u32_b32 v0, -1, 0
	s_mov_b32 s17, 0
	v_cmp_eq_u32_e64 s[6:7], 0, v1
	v_add_u32_e32 v217, s63, v215
	v_add_u32_e32 v218, s64, v215
	v_add_u32_e32 v219, 0, v3
	v_mbcnt_hi_u32_b32 v220, -1, v0
	s_mov_b32 s66, 0
	s_barrier
	s_branch .LBB0_1655

.LBB0_2262:
	s_add_u32 s69, s26, 0x3c000000
	s_addc_u32 s70, s27, 0
	s_lshl_b64 s[14:15], s[14:15], 19
	s_lshl_b64 s[22:23], s[6:7], 7
	s_add_u32 s7, s69, s14
	s_addc_u32 s14, s70, s15
	s_add_u32 s44, s7, s22
	s_addc_u32 s45, s14, s23
	s_lshl_b32 s46, s6, 7
	s_load_dword s6, s[90:91], 0x100
	v_mov_b32_e32 v1, v174
	v_mov_b32_e32 v2, v172
	s_waitcnt lgkmcnt(0)
	s_ashr_i32 s72, s6, 31
	s_add_u32 s6, s26, 0x34000080
	s_addc_u32 s7, s27, 0
	s_lshl_b32 s14, s18, 5
	s_and_b32 s18, s14, 0x60
	s_lshl_b32 s20, s17, 13
	s_lshl_b32 s22, s18, 7
	s_add_u32 s14, s50, 0x80
	s_addc_u32 s15, s51, 0
	s_add_i32 m0, s61, 0x18000
	s_add_i32 s73, s61, 0x8000
	global_load_lds_dwordx4 v2, s[14:15]
	s_add_i32 m0, s61, 0x1a000
	v_mov_b32_e32 v2, v175
	global_load_lds_dwordx4 v1, s[14:15]
	v_mov_b32_e32 v1, v176
	s_mov_b32 m0, s73
	s_add_i32 s74, s61, 0xa000
	s_mov_b32 s76, 0xc0e00000
	global_load_lds_dwordx4 v2, s[6:7]
	s_mov_b32 m0, s74
	v_mov_b32_e32 v2, v174
	global_load_lds_dwordx4 v1, s[6:7]
	s_add_u32 s6, s52, 0x80
	s_addc_u32 s7, s53, 0
	v_mov_b32_e32 v1, v172
	s_add_i32 m0, s61, 0x1c000
	s_mov_b32 s77, 0x40000
	global_load_lds_dwordx4 v1, s[6:7]
	s_add_i32 m0, s61, 0x1e000
	v_and_b32_e32 v1, 15, v0
	global_load_lds_dwordx4 v2, s[6:7]
	v_lshrrev_b32_e32 v2, 1, v0
	v_and_b32_e32 v2, 24, v2
	v_lshlrev_b32_e32 v3, 1, v2
	v_lshlrev_b32_e32 v0, 2, v0
	v_lshl_or_b32 v179, s17, 6, v1
	v_lshl_or_b32 v1, v1, 6, v3
	v_and_b32_e32 v0, 32, v0
	s_cmp_gt_i32 s0, 0
	v_bitop3_b32 v180, v1, s22, v0 bitop3:0xde
	s_waitcnt vmcnt(8)
	s_barrier
	s_waitcnt vmcnt(6)
	s_cselect_b64 s[14:15], -1, 0
	s_add_i32 s75, s0, -2
	v_bitop3_b32 v3, v1, s20, v0 bitop3:0xde
	s_cmpk_lt_u32 s16, 0x100
	v_add_u32_e32 v0, 0, v180
	s_cselect_b64 s[16:17], -1, 0
	v_or_b32_e32 v181, s18, v2
	v_add_u32_e32 v182, 0x10000, v0
	v_add_u32_e32 v183, 0x14000, v0
	v_add_u32_e32 v184, 0, v3
	s_brev_b32 s18, 60
	s_mov_b32 s20, 0xc01d265f
	v_mov_b32_e32 v185, 0x40e00000
	s_mov_b64 s[54:55], s[10:11]
	s_mov_b64 s[56:57], s[10:11]
	s_barrier
	s_branch .LBB0_2265

.LBB0_2349:
	s_add_u32 s64, s26, 0x5e000000
	s_addc_u32 s65, s27, 0
	s_lshl_b64 s[20:21], s[6:7], 8
	s_add_u32 s7, s64, s14
	s_addc_u32 s13, s65, s15
	s_add_u32 s42, s7, s20
	s_addc_u32 s43, s13, s21
	s_lshl_b32 s44, s6, 8
	s_load_dword s6, s[90:91], 0x100
	s_lshl_b32 s46, s12, 8
	s_add_u32 s66, s26, 0xd00000
	s_addc_u32 s67, s27, 0
	s_load_dwordx2 s[12:13], s[90:91], 0xd0
	s_waitcnt lgkmcnt(0)
	s_ashr_i32 s68, s6, 31
	s_lshl_b32 s6, s18, 5
	s_and_b32 s18, s6, 0x60
	s_lshl_b32 s14, s17, 13
	s_lshl_b32 s15, s18, 7
	s_add_u32 s6, s54, 0x80
	s_addc_u32 s7, s55, 0
	v_mov_b32_e32 v1, v181
	v_mov_b32_e32 v2, v179
	s_add_i32 m0, s58, 0x18000
	s_mov_b32 s74, 0x40000
	global_load_lds_dwordx4 v2, s[6:7]
	s_add_i32 m0, s58, 0x1a000
	v_mov_b32_e32 v2, v182
	global_load_lds_dwordx4 v1, s[6:7]
	s_add_u32 s6, s48, 0x80
	s_addc_u32 s7, s49, 0
	s_add_i32 s69, s58, 0x8000
	v_mov_b32_e32 v1, v180
	s_mov_b32 m0, s69
	s_add_i32 s70, s58, 0xa000
	s_mov_b32 s75, 0x50000
	global_load_lds_dwordx4 v1, s[6:7]
	s_mov_b32 m0, s70
	v_mov_b32_e32 v1, v181
	global_load_lds_dwordx4 v2, s[6:7]
	s_add_u32 s6, s54, 0x40080
	s_addc_u32 s7, s55, 0
	v_mov_b32_e32 v2, v179
	s_add_i32 m0, s58, 0x1c000
	s_nop 0
	global_load_lds_dwordx4 v2, s[6:7]
	s_add_i32 m0, s58, 0x1e000
	v_lshrrev_b32_e32 v2, 1, v0
	global_load_lds_dwordx4 v1, s[6:7]
	v_and_b32_e32 v2, 24, v2
	v_and_b32_e32 v1, 15, v0
	v_lshlrev_b32_e32 v3, 1, v2
	v_lshlrev_b32_e32 v0, 2, v0
	v_lshl_or_b32 v183, s17, 6, v1
	v_lshl_or_b32 v1, v1, 6, v3
	v_and_b32_e32 v0, 32, v0
	s_cmp_gt_i32 s0, 0
	v_bitop3_b32 v3, v1, s14, v0 bitop3:0xde
	v_bitop3_b32 v184, v1, s15, v0 bitop3:0xde
	s_cselect_b64 s[14:15], -1, 0
	s_add_i32 s71, s0, -2
	s_waitcnt vmcnt(8)
	s_barrier
	s_waitcnt vmcnt(6)
	s_cmpk_lt_u32 s16, 0x100
	s_cselect_b64 s[16:17], -1, 0
	s_add_i32 s72, 0, 0x10000
	s_add_i32 s73, 0, 0x14000
	v_or_b32_e32 v185, s18, v2
	v_add_u32_e32 v186, s72, v184
	v_add_u32_e32 v187, s73, v184
	v_add_u32_e32 v188, 0, v3
	s_brev_b32 s18, 60
	s_barrier
	s_branch .LBB0_2352
